# baseline (speedup 1.0000x reference)
_Z12giou_partialPK15HIP_vector_typeIfLj4EES2_S2_PKiPS_IfLj2EE:
	s_load_dwordx8 s[16:23], s[0:1], 0x0
	s_load_dwordx2 s[24:25], s[0:1], 0x20
	s_cmpk_ge_u32 s2, 0x100
	s_cbranch_scc1 .Llate_block
	s_movk_i32 s3, 0x200
	s_lshl_b32 s6, s2, 10
	v_cmp_gt_u32_e32 vcc, s3, v0
	v_lshlrev_b32_e32 v11, 4, v0
	v_lshrrev_b32_e32 v1, 6, v0
	v_and_b32_e32 v10, 63, v0
	v_lshl_add_u32 v6, v1, 18, s6
	v_lshlrev_b32_e32 v8, 2, v6
	v_lshl_add_u32 v8, v10, 4, v8
	s_lshl_b32 s7, s2, 14
	v_readfirstlane_b32 s15, v1
	v_add_u32_e32 v43, 0x200, v6
	s_waitcnt lgkmcnt(0)
	s_add_u32 s20, s20, s7
	s_addc_u32 s21, s21, 0
	global_load_dwordx4 v[12:15], v8, s[22:23] nt
	global_load_dwordx4 v[16:19], v8, s[22:23] offset:1024 nt
	global_load_dwordx4 v[26:29], v8, s[22:23] offset:2048 nt
	global_load_dwordx4 v[30:33], v8, s[22:23] offset:3072 nt
	global_load_dwordx4 v[2:5], v11, s[20:21] nt
	v_mov_b32_e32 v7, 0x80
	s_waitcnt vmcnt(0)
	s_sub_u32 s26, 0xff, s2
	s_mul_i32 s26, s26, 0
	s_lshr_b32 s26, s26, 7
	s_min_u32 s26, s26, 64
	s_cmp_eq_u32 s26, 0
	s_cbranch_scc1 .Lhold_done

.LcompB_end:
	s_or_b64 exec, exec, s[10:11]
	s_ashr_i32 s0, s14, 16
	s_add_i32 s3, s3, s0
	s_mov_b32 s28, s3
	ds_write_b128 v11, v[2:5] offset:32768
	s_waitcnt lgkmcnt(0)
	v_mov_b32_e32 v2, 0
	v_cmp_gt_i32_e32 vcc, s27, v10
	s_and_b64 exec, exec, vcc
	s_mov_b64 s[30:31], exec
	s_cbranch_execz .Lskip_issueA
	v_lshlrev_b32_e32 v3, 1, v10
	v_lshl_or_b32 v3, v1, 10, v3
	v_mov_b32_e32 v4, v10
	ds_read_u16 v5, v3
	s_waitcnt lgkmcnt(0)
	v_add_u32_e32 v8, v6, v5
	v_lshlrev_b32_e32 v8, 4, v8
	global_load_dwordx4 v[12:15], v8, s[16:17] nt
	global_load_dwordx4 v[16:19], v8, s[18:19] nt
	v_lshlrev_b32_e32 v5, 4, v5
